# branch GEMM epilogue: entry vmcnt(0) (drained the next unit's in-flight tile DMAs) relaxed to vmcnt(7); gate loads are older than the K-loop's DMAs
# speedup vs baseline: 1.0060x; 1.0060x over previous
.LBB0_998:
	s_waitcnt vmcnt(7)
	v_lshlrev_b32_e32 v175, 16, v0
	v_mul_f32_e32 v175, 0xbfb8aa3b, v175
	v_exp_f32_e32 v175, v175
	v_and_b32_e32 v176, 0xffff0000, v0
	s_waitcnt lgkmcnt(0)
	v_mul_f32_e32 v76, v76, v174
	v_lshlrev_b32_e32 v177, 16, v1
	v_add_f32_e32 v175, 1.0, v175
	v_rcp_f32_e32 v175, v175
	v_and_b32_e32 v178, 0xffff0000, v1
	s_lshl_b32 s19, s28, 8
	s_cmp_eq_u32 s21, 0
	v_mul_f32_e32 v183, v76, v175
	v_fmac_f32_e32 v130, v76, v175
	v_mul_f32_e32 v76, v77, v174
	v_mul_f32_e32 v77, 0xbfb8aa3b, v176
	v_exp_f32_e32 v77, v77
	s_cselect_b64 s[4:5], -1, 0
	v_lshlrev_b32_e32 v179, 16, v2
	v_and_b32_e32 v180, 0xffff0000, v2
	v_add_f32_e32 v77, 1.0, v77
	v_rcp_f32_e32 v77, v77
	v_mul_f32_e32 v72, v72, v174
	v_lshlrev_b32_e32 v181, 16, v3
	v_and_b32_e32 v182, 0xffff0000, v3
	v_mul_f32_e32 v175, v76, v77
	v_fmac_f32_e32 v131, v76, v77
	v_mul_f32_e32 v77, 0xbfb8aa3b, v177
	v_exp_f32_e32 v77, v77
	v_mul_f32_e32 v76, v78, v174
	v_add_u32_e32 v171, s19, v93
	v_cndmask_b32_e64 v130, v130, v183, s[4:5]
	v_add_f32_e32 v77, 1.0, v77
	v_rcp_f32_e32 v77, v77
	v_cndmask_b32_e64 v131, v131, v175, s[4:5]
	s_and_b64 vcc, exec, s[2:3]
	v_lshlrev_b32_e32 v208, 1, v92
	v_mul_f32_e32 v78, v76, v77
	v_fmac_f32_e32 v132, v76, v77
	v_mul_f32_e32 v77, 0xbfb8aa3b, v178
	v_exp_f32_e32 v77, v77
	v_mul_f32_e32 v76, v79, v174
	v_cndmask_b32_e64 v132, v132, v78, s[4:5]
	v_add_f32_e32 v77, 1.0, v77
	v_rcp_f32_e32 v77, v77
	s_nop 0
	v_mul_f32_e32 v78, v76, v77
	v_fmac_f32_e32 v133, v76, v77
	v_mul_f32_e32 v76, 0xbfb8aa3b, v179
	v_exp_f32_e32 v76, v76
	v_cndmask_b32_e64 v133, v133, v78, s[4:5]
	v_add_f32_e32 v76, 1.0, v76
	v_rcp_f32_e32 v76, v76
	s_nop 0
	v_mul_f32_e32 v77, v72, v76
	v_fmac_f32_e32 v126, v72, v76
	v_mul_f32_e32 v72, v73, v174
	v_mul_f32_e32 v73, 0xbfb8aa3b, v180
	v_exp_f32_e32 v73, v73
	v_cndmask_b32_e64 v126, v126, v77, s[4:5]
	v_add_f32_e32 v73, 1.0, v73
	v_rcp_f32_e32 v73, v73
	s_nop 0
	v_mul_f32_e32 v76, v72, v73
	v_fmac_f32_e32 v127, v72, v73
	v_mul_f32_e32 v73, 0xbfb8aa3b, v181
	v_exp_f32_e32 v73, v73
	v_mul_f32_e32 v72, v74, v174
	v_cndmask_b32_e64 v127, v127, v76, s[4:5]
	v_add_f32_e32 v73, 1.0, v73
	v_rcp_f32_e32 v73, v73
	s_nop 0
	v_mul_f32_e32 v74, v72, v73
	v_fmac_f32_e32 v128, v72, v73
	v_mul_f32_e32 v73, 0xbfb8aa3b, v182
	v_exp_f32_e32 v73, v73
	v_mul_f32_e32 v72, v75, v174
	v_cndmask_b32_e64 v128, v128, v74, s[4:5]
	v_add_f32_e32 v73, 1.0, v73
	v_rcp_f32_e32 v73, v73
	s_nop 0
	v_mul_f32_e32 v74, v72, v73
	v_fmac_f32_e32 v129, v72, v73
	v_cndmask_b32_e64 v129, v129, v74, s[4:5]
	s_cbranch_vccnz .LBB0_1000
	v_mov_b64_e32 v[76:77], s[8:9]
	v_mad_i64_i32 v[76:77], s[6:7], v171, s62, v[76:77]
	s_ashr_i32 s21, s20, 31
	v_lshl_add_u64 v[76:77], s[20:21], 1, v[76:77]
	s_lshl_b32 s68, s38, 1
	v_lshl_add_u64 v[76:77], v[76:77], 0, s[68:69]
	v_lshl_add_u64 v[76:77], v[76:77], 0, v[208:209]
	s_mov_b64 s[6:7], 0xc00
	v_cvt_pk_bf16_f32 v72, v130, v131
	v_cvt_pk_bf16_f32 v73, v132, v133
	v_cvt_pk_bf16_f32 v74, v126, v127
	v_cvt_pk_bf16_f32 v75, v128, v129
	v_lshl_add_u64 v[76:77], v[76:77], 0, s[6:7]
	global_store_dwordx4 v[76:77], v[72:75], off sc1
	s_nop 1
